# P7 router-weight LDS staging loop: 8 loads per iteration issued together with counted waits (was 4 serial load pairs), on top of v7_krope
# speedup vs baseline: 1.0079x; 1.0002x over previous
.LBB0_1502:
	v_lshlrev_b32_e32 v10, 4, v5
	v_lshlrev_b32_e32 v11, 4, v4
	v_and_b32_e32 v18, 0x300, v10
	v_and_b32_e32 v19, 0x300, v11
	v_mov_b32_e32 v10, v4
	v_mov_b32_e32 v12, v5
	v_ashrrev_i32_e32 v11, 31, v10
	v_ashrrev_i32_e32 v13, 31, v12
	v_lshl_add_u64 v[14:15], v[10:11], 2, s[38:39]
	v_lshl_add_u64 v[16:17], v[12:13], 2, s[38:39]
	global_load_dword v28, v[14:15], off
	global_load_dword v29, v[16:17], off
	v_add_u32_e32 v10, 0x400, v4
	v_add_u32_e32 v12, 0x400, v5
	v_ashrrev_i32_e32 v11, 31, v10
	v_ashrrev_i32_e32 v13, 31, v12
	v_lshl_add_u64 v[14:15], v[10:11], 2, s[38:39]
	v_lshl_add_u64 v[16:17], v[12:13], 2, s[38:39]
	global_load_dword v30, v[14:15], off
	global_load_dword v31, v[16:17], off
	v_add_u32_e32 v10, 0x800, v4
	v_add_u32_e32 v12, 0x800, v5
	v_ashrrev_i32_e32 v11, 31, v10
	v_ashrrev_i32_e32 v13, 31, v12
	v_lshl_add_u64 v[14:15], v[10:11], 2, s[38:39]
	v_lshl_add_u64 v[16:17], v[12:13], 2, s[38:39]
	global_load_dword v32, v[14:15], off
	global_load_dword v33, v[16:17], off
	v_add_u32_e32 v10, 0xc00, v4
	v_add_u32_e32 v12, 0xc00, v5
	v_ashrrev_i32_e32 v11, 31, v10
	v_ashrrev_i32_e32 v13, 31, v12
	v_lshl_add_u64 v[14:15], v[10:11], 2, s[38:39]
	v_lshl_add_u64 v[16:17], v[12:13], 2, s[38:39]
	global_load_dword v34, v[14:15], off
	global_load_dword v35, v[16:17], off
	v_add_u32_e32 v8, -4, v8
	v_cmp_eq_u32_e32 vcc, 0, v8
	s_or_b64 s[42:43], vcc, s[42:43]
	v_ashrrev_i32_e32 v10, 6, v4
	v_ashrrev_i32_e32 v11, 6, v5
	v_add_u32_e32 v10, v19, v10
	v_add_u32_e32 v12, v18, v11
	v_mad_u64_u32 v[10:11], s[0:1], v10, s6, v[2:3]
	v_mad_u64_u32 v[12:13], s[0:1], v12, s6, v[2:3]
	s_waitcnt vmcnt(7)
	ds_write_b32 v10, v28
	s_waitcnt vmcnt(6)
	ds_write_b32 v12, v29
	v_add_u32_e32 v10, 0x400, v4
	v_add_u32_e32 v12, 0x400, v5
	v_ashrrev_i32_e32 v10, 6, v10
	v_ashrrev_i32_e32 v11, 6, v12
	v_add_u32_e32 v10, v19, v10
	v_add_u32_e32 v12, v18, v11
	v_mad_u64_u32 v[10:11], s[0:1], v10, s6, v[2:3]
	v_mad_u64_u32 v[12:13], s[0:1], v12, s6, v[2:3]
	s_waitcnt vmcnt(5)
	ds_write_b32 v10, v30
	s_waitcnt vmcnt(4)
	ds_write_b32 v12, v31
	v_add_u32_e32 v10, 0x800, v4
	v_add_u32_e32 v12, 0x800, v5
	v_ashrrev_i32_e32 v10, 6, v10
	v_ashrrev_i32_e32 v11, 6, v12
	v_add_u32_e32 v10, v19, v10
	v_add_u32_e32 v12, v18, v11
	v_mad_u64_u32 v[10:11], s[0:1], v10, s6, v[2:3]
	v_mad_u64_u32 v[12:13], s[0:1], v12, s6, v[2:3]
	s_waitcnt vmcnt(3)
	ds_write_b32 v10, v32
	s_waitcnt vmcnt(2)
	ds_write_b32 v12, v33
	v_add_u32_e32 v10, 0xc00, v4
	v_add_u32_e32 v12, 0xc00, v5
	v_ashrrev_i32_e32 v10, 6, v10
	v_ashrrev_i32_e32 v11, 6, v12
	v_add_u32_e32 v10, v19, v10
	v_add_u32_e32 v12, v18, v11
	v_mad_u64_u32 v[10:11], s[0:1], v10, s6, v[2:3]
	v_mad_u64_u32 v[12:13], s[0:1], v12, s6, v[2:3]
	s_waitcnt vmcnt(1)
	ds_write_b32 v10, v34
	s_waitcnt vmcnt(0)
	ds_write_b32 v12, v35
	v_add_u32_e32 v5, 0x1000, v5
	v_add_u32_e32 v4, 0x1000, v4
	s_andn2_b64 exec, exec, s[42:43]
	s_cbranch_execnz .LBB0_1502
	s_or_b64 exec, exec, s[42:43]
